# v023 + skip the now-empty phase-7 tail queue loop
# baseline (speedup 1.0000x reference)
.LBB0_734:
	s_branch .LBB0_746
	s_add_u32 s10, s48, 0xc000
	v_lshrrev_b32_e32 v8, 6, v0
	v_and_b32_e32 v2, 0xfc, v1
	s_addc_u32 s11, s49, 0
	v_mul_u32_u24_e32 v1, 0x410, v8
	v_lshlrev_b32_e32 v4, 2, v2
	s_mov_b32 s4, 0x10400
	v_lshrrev_b32_e32 v39, 1, v0
	v_and_b32_e32 v5, 1, v0
	s_add_u32 s22, s16, 0x5ee00000
	v_add3_u32 v1, 0, v1, v4
	v_lshlrev_b32_e32 v4, 6, v5
	v_mad_u32_u24 v5, v5, s4, 0
	v_lshlrev_b32_e32 v7, 2, v39
	v_lshrrev_b32_e32 v6, 2, v0
	s_addc_u32 s23, s17, 0
	v_mov_b32_e32 v3, 0
	v_add3_u32 v40, v5, v4, v7
	v_lshlrev_b32_e32 v7, 7, v39
	s_movk_i32 s4, 0xff
	s_add_i32 s24, 0, 0x27fd0
	s_mov_b32 s5, 0
	v_cmp_eq_u32_e64 s[2:3], 0, v0
	v_or_b32_e32 v9, 8, v8
	v_add_u32_e32 v10, 0x2080, v1
	v_or_b32_e32 v11, 16, v8
	v_add_u32_e32 v12, 0x4100, v1
	v_or_b32_e32 v13, 24, v8
	v_add_u32_e32 v14, 0x6180, v1
	v_or_b32_e32 v15, 32, v8
	v_add_u32_e32 v16, 0x8200, v1
	v_or_b32_e32 v17, 40, v8
	v_add_u32_e32 v18, 0xa280, v1
	v_or_b32_e32 v19, 48, v8
	v_add_u32_e32 v20, 0xc300, v1
	v_or_b32_e32 v21, 56, v8
	v_add_u32_e32 v22, 0xe380, v1
	v_or_b32_e32 v23, 64, v8
	v_add_u32_e32 v24, 0x10400, v1
	v_or_b32_e32 v25, 0x48, v8
	v_add_u32_e32 v26, 0x12480, v1
	v_or_b32_e32 v27, 0x50, v8
	v_add_u32_e32 v28, 0x14500, v1
	v_or_b32_e32 v29, 0x58, v8
	v_add_u32_e32 v30, 0x16580, v1
	v_or_b32_e32 v31, 0x60, v8
	v_add_u32_e32 v32, 0x18600, v1
	v_or_b32_e32 v33, 0x68, v8
	v_add_u32_e32 v34, 0x1a680, v1
	v_or_b32_e32 v35, 0x70, v8
	v_add_u32_e32 v36, 0x1c700, v1
	v_or_b32_e32 v37, 0x78, v8
	v_add_u32_e32 v38, 0x1e7c0, v1
	v_mov_b32_e32 v5, v3
	v_bitop3_b32 v41, v7, s4, v6 bitop3:0xc8
	v_mov_b32_e32 v42, s24
	s_movk_i32 s25, 0xffff
	v_lshlrev_b32_e32 v2, 2, v2
	s_branch .LBB0_737
